# baseline (speedup 1.0000x reference)
.LBB0_46:
	s_or_b64 exec, exec, s[4:5]
	v_lshlrev_b32_e32 v2, 5, v44
	s_waitcnt lgkmcnt(0)
	s_barrier
	ds_read_b128 v[14:17], v2 offset:20480
	ds_read_b128 v[2:5], v2 offset:20496
	v_mov_b32_e32 v41, 0
	v_lshlrev_b32_e32 v40, 4, v1
	s_waitcnt lgkmcnt(1)
	v_cmp_gt_i32_e64 s[16:17], 0, v14
	v_max_i32_e32 v42, 0, v14
	v_lshl_add_u32 v42, v42, 10, v40
	global_load_dwordx4 v[48:51], v42, s[24:25] nt
	v_cmp_gt_i32_e64 s[14:15], 0, v15
	v_max_i32_e32 v43, 0, v15
	v_lshl_add_u32 v43, v43, 10, v40
	global_load_dwordx4 v[34:37], v43, s[24:25] nt
	v_cmp_gt_i32_e64 s[12:13], 0, v16
	v_max_i32_e32 v42, 0, v16
	v_lshl_add_u32 v42, v42, 10, v40
	global_load_dwordx4 v[30:33], v42, s[24:25] nt
	v_cmp_gt_i32_e64 s[10:11], 0, v17
	v_max_i32_e32 v43, 0, v17
	v_lshl_add_u32 v43, v43, 10, v40
	global_load_dwordx4 v[26:29], v43, s[24:25] nt
	s_waitcnt lgkmcnt(0)
	v_cmp_gt_i32_e64 s[8:9], 0, v2
	v_max_i32_e32 v42, 0, v2
	v_lshl_add_u32 v42, v42, 10, v40
	global_load_dwordx4 v[22:25], v42, s[24:25] nt
	v_cmp_gt_i32_e64 s[6:7], 0, v3
	v_max_i32_e32 v43, 0, v3
	v_lshl_add_u32 v43, v43, 10, v40
	global_load_dwordx4 v[18:21], v43, s[24:25] nt
	v_cmp_gt_i32_e64 s[4:5], 0, v4
	v_max_i32_e32 v42, 0, v4
	v_lshl_add_u32 v42, v42, 10, v40
	global_load_dwordx4 v[10:13], v42, s[24:25] nt
	v_cmp_gt_i32_e64 s[2:3], 0, v5
	v_max_i32_e32 v43, 0, v5
	v_lshl_add_u32 v43, v43, 10, v40
	global_load_dwordx4 v[6:9], v43, s[24:25] nt
	v_lshlrev_b32_e32 v1, 8, v0
	v_lshlrev_b32_e32 v0, 3, v0
	s_movk_i32 s19, 0x3c00
	v_and_b32_e32 v0, 8, v0
	v_and_or_b32 v46, v1, s19, v0
	s_mul_i32 s18, s20, 0x4080
	s_mul_hi_u32 s24, s20, 0x4080
	s_add_u32 s18, s22, s18
	v_lshlrev_b32_e32 v39, 3, v44
	v_and_b32_e32 v41, 32, v38
	s_addc_u32 s19, s23, s24
	s_add_u32 s22, s18, 0x4000
	s_addc_u32 s23, s19, 0
	v_add_u32_e32 v60, v39, v41
	v_lshl_add_u32 v60, v60, 4, v46
	v_mov_b32_e32 v66, 0x7f800000
	s_waitcnt vmcnt(7)
	v_cndmask_b32_e64 v48, v48, 0, s[16:17]
	v_cndmask_b32_e64 v49, v49, 0, s[16:17]
	v_cndmask_b32_e64 v50, v50, 0, s[16:17]
	v_cndmask_b32_e64 v51, v51, 0, s[16:17]
	v_pk_mul_f32 v[62:63], v[48:49], v[48:49]
	v_pk_mul_f32 v[64:65], v[50:51], v[50:51]
	v_add_f32_e32 v52, v62, v63
	v_add_f32_e32 v52, v52, v64
	v_add_f32_e32 v52, v52, v65
	v_cvt_pk_f16_f32 v62, v48, v49
	v_cvt_pk_f16_f32 v63, v50, v51
	ds_write_b64 v60, v[62:63]
	s_waitcnt vmcnt(6)
	v_cndmask_b32_e64 v34, v34, 0, s[14:15]
	v_cndmask_b32_e64 v35, v35, 0, s[14:15]
	v_cndmask_b32_e64 v36, v36, 0, s[14:15]
	v_cndmask_b32_e64 v37, v37, 0, s[14:15]
	v_pk_mul_f32 v[62:63], v[34:35], v[34:35]
	v_pk_mul_f32 v[64:65], v[36:37], v[36:37]
	v_add_f32_e32 v53, v62, v63
	v_add_f32_e32 v53, v53, v64
	v_add_f32_e32 v53, v53, v65
	v_cvt_pk_f16_f32 v62, v34, v35
	v_cvt_pk_f16_f32 v63, v36, v37
	ds_write_b64 v60, v[62:63] offset:16
	s_waitcnt vmcnt(5)
	v_cndmask_b32_e64 v30, v30, 0, s[12:13]
	v_cndmask_b32_e64 v31, v31, 0, s[12:13]
	v_cndmask_b32_e64 v32, v32, 0, s[12:13]
	v_cndmask_b32_e64 v33, v33, 0, s[12:13]
	v_pk_mul_f32 v[62:63], v[30:31], v[30:31]
	v_pk_mul_f32 v[64:65], v[32:33], v[32:33]
	v_add_f32_e32 v54, v62, v63
	v_add_f32_e32 v54, v54, v64
	v_add_f32_e32 v54, v54, v65
	v_cvt_pk_f16_f32 v62, v30, v31
	v_cvt_pk_f16_f32 v63, v32, v33
	ds_write_b64 v60, v[62:63] offset:32
	s_waitcnt vmcnt(4)
	v_cndmask_b32_e64 v26, v26, 0, s[10:11]
	v_cndmask_b32_e64 v27, v27, 0, s[10:11]
	v_cndmask_b32_e64 v28, v28, 0, s[10:11]
	v_cndmask_b32_e64 v29, v29, 0, s[10:11]
	v_pk_mul_f32 v[62:63], v[26:27], v[26:27]
	v_pk_mul_f32 v[64:65], v[28:29], v[28:29]
	v_add_f32_e32 v55, v62, v63
	v_add_f32_e32 v55, v55, v64
	v_add_f32_e32 v55, v55, v65
	v_cvt_pk_f16_f32 v62, v26, v27
	v_cvt_pk_f16_f32 v63, v28, v29
	ds_write_b64 v60, v[62:63] offset:48
	s_waitcnt vmcnt(3)
	v_cndmask_b32_e64 v22, v22, 0, s[8:9]
	v_cndmask_b32_e64 v23, v23, 0, s[8:9]
	v_cndmask_b32_e64 v24, v24, 0, s[8:9]
	v_cndmask_b32_e64 v25, v25, 0, s[8:9]
	v_pk_mul_f32 v[62:63], v[22:23], v[22:23]
	v_pk_mul_f32 v[64:65], v[24:25], v[24:25]
	v_add_f32_e32 v56, v62, v63
	v_add_f32_e32 v56, v56, v64
	v_add_f32_e32 v56, v56, v65
	v_cvt_pk_f16_f32 v62, v22, v23
	v_cvt_pk_f16_f32 v63, v24, v25
	ds_write_b64 v60, v[62:63] offset:64
	s_waitcnt vmcnt(2)
	v_cndmask_b32_e64 v18, v18, 0, s[6:7]
	v_cndmask_b32_e64 v19, v19, 0, s[6:7]
	v_cndmask_b32_e64 v20, v20, 0, s[6:7]
	v_cndmask_b32_e64 v21, v21, 0, s[6:7]
	v_pk_mul_f32 v[62:63], v[18:19], v[18:19]
	v_pk_mul_f32 v[64:65], v[20:21], v[20:21]
	v_add_f32_e32 v57, v62, v63
	v_add_f32_e32 v57, v57, v64
	v_add_f32_e32 v57, v57, v65
	v_cvt_pk_f16_f32 v62, v18, v19
	v_cvt_pk_f16_f32 v63, v20, v21
	ds_write_b64 v60, v[62:63] offset:80
	s_waitcnt vmcnt(1)
	v_cndmask_b32_e64 v10, v10, 0, s[4:5]
	v_cndmask_b32_e64 v11, v11, 0, s[4:5]
	v_cndmask_b32_e64 v12, v12, 0, s[4:5]
	v_cndmask_b32_e64 v13, v13, 0, s[4:5]
	v_pk_mul_f32 v[62:63], v[10:11], v[10:11]
	v_pk_mul_f32 v[64:65], v[12:13], v[12:13]
	v_add_f32_e32 v58, v62, v63
	v_add_f32_e32 v58, v58, v64
	v_add_f32_e32 v58, v58, v65
	v_cvt_pk_f16_f32 v62, v10, v11
	v_cvt_pk_f16_f32 v63, v12, v13
	ds_write_b64 v60, v[62:63] offset:96
	s_waitcnt vmcnt(0)
	v_cndmask_b32_e64 v6, v6, 0, s[2:3]
	v_cndmask_b32_e64 v7, v7, 0, s[2:3]
	v_cndmask_b32_e64 v8, v8, 0, s[2:3]
	v_cndmask_b32_e64 v9, v9, 0, s[2:3]
	v_pk_mul_f32 v[62:63], v[6:7], v[6:7]
	v_pk_mul_f32 v[64:65], v[8:9], v[8:9]
	v_add_f32_e32 v59, v62, v63
	v_add_f32_e32 v59, v59, v64
	v_add_f32_e32 v59, v59, v65
	v_cvt_pk_f16_f32 v62, v6, v7
	v_cvt_pk_f16_f32 v63, v8, v9
	ds_write_b64 v60, v[62:63] offset:112
	v_add_f32_dpp v52, v52, v52 quad_perm:[1,0,3,2] row_mask:0xf bank_mask:0xf bound_ctrl:1
	v_add_f32_dpp v53, v53, v53 quad_perm:[1,0,3,2] row_mask:0xf bank_mask:0xf bound_ctrl:1
	v_add_f32_dpp v54, v54, v54 quad_perm:[1,0,3,2] row_mask:0xf bank_mask:0xf bound_ctrl:1
	v_add_f32_dpp v55, v55, v55 quad_perm:[1,0,3,2] row_mask:0xf bank_mask:0xf bound_ctrl:1
	v_add_f32_dpp v56, v56, v56 quad_perm:[1,0,3,2] row_mask:0xf bank_mask:0xf bound_ctrl:1
	v_add_f32_dpp v57, v57, v57 quad_perm:[1,0,3,2] row_mask:0xf bank_mask:0xf bound_ctrl:1
	v_add_f32_dpp v58, v58, v58 quad_perm:[1,0,3,2] row_mask:0xf bank_mask:0xf bound_ctrl:1
	v_add_f32_dpp v59, v59, v59 quad_perm:[1,0,3,2] row_mask:0xf bank_mask:0xf bound_ctrl:1
	v_add_f32_dpp v52, v52, v52 quad_perm:[2,3,0,1] row_mask:0xf bank_mask:0xf bound_ctrl:1
	v_add_f32_dpp v53, v53, v53 quad_perm:[2,3,0,1] row_mask:0xf bank_mask:0xf bound_ctrl:1
	v_add_f32_dpp v54, v54, v54 quad_perm:[2,3,0,1] row_mask:0xf bank_mask:0xf bound_ctrl:1
	v_add_f32_dpp v55, v55, v55 quad_perm:[2,3,0,1] row_mask:0xf bank_mask:0xf bound_ctrl:1
	v_add_f32_dpp v56, v56, v56 quad_perm:[2,3,0,1] row_mask:0xf bank_mask:0xf bound_ctrl:1
	v_add_f32_dpp v57, v57, v57 quad_perm:[2,3,0,1] row_mask:0xf bank_mask:0xf bound_ctrl:1
	v_add_f32_dpp v58, v58, v58 quad_perm:[2,3,0,1] row_mask:0xf bank_mask:0xf bound_ctrl:1
	v_add_f32_dpp v59, v59, v59 quad_perm:[2,3,0,1] row_mask:0xf bank_mask:0xf bound_ctrl:1
	v_add_f32_dpp v52, v52, v52 row_half_mirror row_mask:0xf bank_mask:0xf bound_ctrl:1
	v_add_f32_dpp v53, v53, v53 row_half_mirror row_mask:0xf bank_mask:0xf bound_ctrl:1
	v_add_f32_dpp v54, v54, v54 row_half_mirror row_mask:0xf bank_mask:0xf bound_ctrl:1
	v_add_f32_dpp v55, v55, v55 row_half_mirror row_mask:0xf bank_mask:0xf bound_ctrl:1
	v_add_f32_dpp v56, v56, v56 row_half_mirror row_mask:0xf bank_mask:0xf bound_ctrl:1
	v_add_f32_dpp v57, v57, v57 row_half_mirror row_mask:0xf bank_mask:0xf bound_ctrl:1
	v_add_f32_dpp v58, v58, v58 row_half_mirror row_mask:0xf bank_mask:0xf bound_ctrl:1
	v_add_f32_dpp v59, v59, v59 row_half_mirror row_mask:0xf bank_mask:0xf bound_ctrl:1
	v_add_f32_dpp v52, v52, v52 row_mirror row_mask:0xf bank_mask:0xf bound_ctrl:1
	v_add_f32_dpp v53, v53, v53 row_mirror row_mask:0xf bank_mask:0xf bound_ctrl:1
	v_add_f32_dpp v54, v54, v54 row_mirror row_mask:0xf bank_mask:0xf bound_ctrl:1
	v_add_f32_dpp v55, v55, v55 row_mirror row_mask:0xf bank_mask:0xf bound_ctrl:1
	v_add_f32_dpp v56, v56, v56 row_mirror row_mask:0xf bank_mask:0xf bound_ctrl:1
	v_add_f32_dpp v57, v57, v57 row_mirror row_mask:0xf bank_mask:0xf bound_ctrl:1
	v_add_f32_dpp v58, v58, v58 row_mirror row_mask:0xf bank_mask:0xf bound_ctrl:1
	v_add_f32_dpp v59, v59, v59 row_mirror row_mask:0xf bank_mask:0xf bound_ctrl:1
	v_add_f32_dpp v52, v52, v52 row_bcast:15 row_mask:0xa bank_mask:0xf
	v_add_f32_dpp v53, v53, v53 row_bcast:15 row_mask:0xa bank_mask:0xf
	v_add_f32_dpp v54, v54, v54 row_bcast:15 row_mask:0xa bank_mask:0xf
	v_add_f32_dpp v55, v55, v55 row_bcast:15 row_mask:0xa bank_mask:0xf
	v_add_f32_dpp v56, v56, v56 row_bcast:15 row_mask:0xa bank_mask:0xf
	v_add_f32_dpp v57, v57, v57 row_bcast:15 row_mask:0xa bank_mask:0xf
	v_add_f32_dpp v58, v58, v58 row_bcast:15 row_mask:0xa bank_mask:0xf
	v_add_f32_dpp v59, v59, v59 row_bcast:15 row_mask:0xa bank_mask:0xf
	v_add_f32_dpp v52, v52, v52 row_bcast:31 row_mask:0xc bank_mask:0xf
	v_add_f32_dpp v53, v53, v53 row_bcast:31 row_mask:0xc bank_mask:0xf
	v_add_f32_dpp v54, v54, v54 row_bcast:31 row_mask:0xc bank_mask:0xf
	v_add_f32_dpp v55, v55, v55 row_bcast:31 row_mask:0xc bank_mask:0xf
	v_add_f32_dpp v56, v56, v56 row_bcast:31 row_mask:0xc bank_mask:0xf
	v_add_f32_dpp v57, v57, v57 row_bcast:31 row_mask:0xc bank_mask:0xf
	v_add_f32_dpp v58, v58, v58 row_bcast:31 row_mask:0xc bank_mask:0xf
	v_add_f32_dpp v59, v59, v59 row_bcast:31 row_mask:0xc bank_mask:0xf
	v_pk_add_f32 v[0:1], v[48:49], 0 op_sel_hi:[1,0]
	v_pk_add_f32 v[2:3], v[50:51], 0 op_sel_hi:[1,0]
	v_pk_add_f32 v[0:1], v[0:1], v[34:35]
	v_pk_add_f32 v[2:3], v[2:3], v[36:37]
	v_pk_add_f32 v[0:1], v[0:1], v[30:31]
	v_pk_add_f32 v[2:3], v[2:3], v[32:33]
	v_pk_add_f32 v[0:1], v[0:1], v[26:27]
	v_pk_add_f32 v[2:3], v[2:3], v[28:29]
	v_pk_add_f32 v[0:1], v[0:1], v[22:23]
	v_pk_add_f32 v[2:3], v[2:3], v[24:25]
	v_pk_add_f32 v[0:1], v[0:1], v[18:19]
	v_pk_add_f32 v[2:3], v[2:3], v[20:21]
	v_pk_add_f32 v[0:1], v[0:1], v[10:11]
	v_pk_add_f32 v[2:3], v[2:3], v[12:13]
	v_pk_add_f32 v[0:1], v[0:1], v[6:7]
	v_pk_add_f32 v[2:3], v[2:3], v[8:9]
	s_mov_b64 s[24:25], exec
	s_mov_b32 exec_lo, 0
	s_brev_b32 exec_hi, 1
	v_cndmask_b32_e64 v52, v52, v66, s[16:17]
	v_cndmask_b32_e64 v53, v53, v66, s[14:15]
	v_cndmask_b32_e64 v54, v54, v66, s[12:13]
	v_cndmask_b32_e64 v55, v55, v66, s[10:11]
	v_cndmask_b32_e64 v56, v56, v66, s[8:9]
	v_cndmask_b32_e64 v57, v57, v66, s[6:7]
	v_cndmask_b32_e64 v58, v58, v66, s[4:5]
	v_cndmask_b32_e64 v59, v59, v66, s[2:3]
	v_lshlrev_b32_e32 v61, 2, v39
	global_store_dwordx4 v61, v[52:55], s[22:23]
	global_store_dwordx4 v61, v[56:59], s[22:23] offset:16
	s_mov_b64 exec, s[24:25]
	s_load_dwordx2 s[6:7], s[0:1], 0x18
	v_lshl_or_b32 v4, v44, 10, v40
	ds_write_b128 v4, v[0:3] offset:16384
	s_waitcnt lgkmcnt(0)
	s_barrier
	ds_read_b128 v[0:3], v38
	ds_read_b128 v[4:7], v38 offset:4096
	v_mov_b32_e32 v39, 0
	v_lshl_add_u64 v[8:9], s[18:19], 0, v[38:39]
	s_movk_i32 s0, 0x2000
	s_waitcnt lgkmcnt(1)
	global_store_dwordx4 v38, v[0:3], s[18:19]
	ds_read_b128 v[0:3], v38 offset:8192
	v_add_co_u32_e32 v10, vcc, s0, v8
	s_movk_i32 s0, 0x3000
	s_nop 0
	v_addc_co_u32_e32 v11, vcc, 0, v9, vcc
	s_waitcnt lgkmcnt(1)
	global_store_dwordx4 v[10:11], v[4:7], off offset:-4096
	ds_read_b128 v[4:7], v38 offset:12288
	s_waitcnt lgkmcnt(1)
	global_store_dwordx4 v[10:11], v[0:3], off
	ds_read2st64_b32 v[0:1], v45 offset0:64 offset1:68
	ds_read2st64_b32 v[2:3], v45 offset0:72 offset1:76
	v_add_co_u32_e32 v8, vcc, s0, v8
	s_lshl_b64 s[0:1], s[20:21], 10
	s_waitcnt lgkmcnt(1)
	v_add_f32_e32 v0, v0, v1
	s_waitcnt lgkmcnt(0)
	v_add_f32_e32 v0, v0, v2
	s_add_u32 s0, s6, s0
	v_addc_co_u32_e32 v9, vcc, 0, v9, vcc
	v_add_f32_e32 v0, v0, v3
	s_addc_u32 s1, s7, s1
	global_store_dwordx4 v[8:9], v[4:7], off
	global_store_dword v45, v0, s[0:1]

.LBB1_3:
	s_mul_i32 s0, s7, s2
	s_sub_i32 s0, s6, s0
	s_add_i32 s1, s7, 1
	s_sub_i32 s6, s0, s2
	s_cmp_ge_u32 s0, s2
	s_cselect_b32 s1, s1, s7
	s_cselect_b32 s0, s6, s0
	s_add_i32 s6, s1, 1
	s_cmp_ge_u32 s0, s2
	s_cselect_b32 s0, s6, s1
	s_xor_b32 s0, s0, s5
	s_sub_i32 s0, s0, s5
	s_mul_i32 s79, s0, s76
	s_add_i32 s0, s79, s0
	s_lshl_b32 s33, s59, 7
	s_add_i32 s4, s33, s4
	s_min_i32 s80, s0, s3
	s_mul_i32 s0, s72, 0x4080
	s_mul_hi_i32 s1, s72, 0x4080
	s_add_u32 s0, s62, s0
	s_addc_u32 s1, s63, s1
	s_mul_i32 s2, s79, 0x4080
	v_and_b32_e32 v114, 63, v0
	s_mul_hi_i32 s3, s79, 0x4080
	s_add_u32 s2, s0, s2
	s_addc_u32 s3, s1, s3
	v_lshlrev_b32_e32 v108, 4, v114
	v_lshl_add_u64 v[2:3], s[2:3], 0, v[108:109]
	s_ashr_i32 s2, s4, 5
	s_mul_hi_i32 s3, s2, 0x4080
	s_mulk_i32 s2, 0x4080
	v_lshrrev_b32_e32 v27, 6, v0
	s_add_u32 s2, s62, s2
	s_addc_u32 s3, s63, s3
	v_lshlrev_b32_e32 v6, 10, v27
	v_lshl_add_u64 v[4:5], s[2:3], 0, v[108:109]
	v_mov_b32_e32 v7, v109
	v_lshl_add_u64 v[8:9], v[2:3], 0, v[6:7]
	v_lshl_add_u64 v[10:11], v[4:5], 0, v[6:7]
	v_add_u32_e32 v14, 0x3000, v6
	v_add_u32_e32 v16, 0x6000, v6
	v_add_u32_e32 v18, 0x9000, v6
	v_bfe_u32 v119, v0, 6, 2
	v_and_b32_e32 v118, 31, v0
	s_mov_b64 s[62:63], 0xc00
	v_add_u32_e32 v15, 0x15000, v6
	s_mov_b64 s[2:3], 0xc00
	v_lshl_add_u64 v[12:13], v[10:11], 0, s[2:3]
	v_readfirstlane_b32 s4, v15
	s_mov_b32 m0, s4
	s_nop 0
	global_load_lds_dwordx4 v[12:13], off
	v_add_u32_e32 v15, 0x18000, v6
	s_mov_b64 s[2:3], 0x3c00
	v_lshl_add_u64 v[12:13], v[10:11], 0, s[2:3]
	v_readfirstlane_b32 s4, v15
	s_mov_b32 m0, s4
	s_nop 0
	global_load_lds_dwordx4 v[12:13], off
	v_add_u32_e32 v15, 0x1b000, v6
	s_mov_b64 s[2:3], 0x6c00
	v_lshl_add_u64 v[12:13], v[10:11], 0, s[2:3]
	v_readfirstlane_b32 s4, v15
	s_mov_b32 m0, s4
	s_nop 0
	global_load_lds_dwordx4 v[12:13], off
	v_add_u32_e32 v15, 0x1e000, v6
	s_mov_b64 s[2:3], 0x9c00
	v_lshl_add_u64 v[12:13], v[10:11], 0, s[2:3]
	v_readfirstlane_b32 s4, v15
	s_mov_b32 m0, s4
	s_nop 0
	global_load_lds_dwordx4 v[12:13], off
	v_add_u32_e32 v15, 0x21000, v6
	s_mov_b64 s[2:3], 0xcc00
	v_lshl_add_u64 v[12:13], v[10:11], 0, s[2:3]
	v_readfirstlane_b32 s4, v15
	s_mov_b32 m0, s4
	s_nop 0
	global_load_lds_dwordx4 v[12:13], off
	v_or_b32_e32 v12, 0x90, v27
	v_min_u32_e32 v12, 0x91, v12
	v_lshlrev_b32_e32 v12, 10, v12
	v_mov_b32_e32 v13, v109
	s_nop 0
	v_readfirstlane_b32 s4, v12
	v_lshl_add_u64 v[12:13], v[4:5], 0, v[12:13]
	s_mov_b32 s2, 0xfffebc00
	s_mov_b32 s3, -1
	v_lshl_add_u64 v[12:13], v[12:13], 0, s[2:3]
	s_mov_b32 m0, s4
	s_nop 0
	global_load_lds_dwordx4 v[12:13], off
	s_movk_i32 s2, 0xdc00
	s_mov_b32 s3, -1
	v_lshl_add_u64 v[12:13], v[10:11], 0, s[2:3]
	s_mov_b64 s[2:3], 0x12000
	v_lshl_add_u64 v[142:143], v[8:9], 0, s[2:3]
	s_movk_i32 s4, 0x23f
	v_cmp_lt_u32_e32 vcc, s4, v0
	v_add_u32_e32 v15, 0x12000, v6
	s_nop 0
	v_cndmask_b32_e32 v12, v142, v12, vcc
	v_cndmask_b32_e32 v13, v143, v13, vcc
	v_readfirstlane_b32 s4, v15
	s_mov_b32 m0, s4
	s_nop 0
	global_load_lds_dwordx4 v[12:13], off
	v_mov_b32_e32 v15, v6
	v_mov_b32_e32 v12, v8
	v_mov_b32_e32 v13, v9
	v_readfirstlane_b32 s4, v15
	s_mov_b32 m0, s4
	s_nop 0
	global_load_lds_dwordx4 v[12:13], off
	v_add_u32_e32 v15, 0x3000, v6
	s_mov_b64 s[2:3], 0x3000
	v_lshl_add_u64 v[12:13], v[8:9], 0, s[2:3]
	v_readfirstlane_b32 s4, v15
	s_mov_b32 m0, s4
	s_nop 0
	global_load_lds_dwordx4 v[12:13], off
	v_add_u32_e32 v15, 0x6000, v6
	s_mov_b64 s[2:3], 0x6000
	v_lshl_add_u64 v[12:13], v[8:9], 0, s[2:3]
	v_readfirstlane_b32 s4, v15
	s_mov_b32 m0, s4
	s_nop 0
	global_load_lds_dwordx4 v[12:13], off
	v_add_u32_e32 v15, 0x9000, v6
	s_mov_b64 s[2:3], 0x9000
	v_lshl_add_u64 v[12:13], v[8:9], 0, s[2:3]
	v_readfirstlane_b32 s4, v15
	s_mov_b32 m0, s4
	s_nop 0
	global_load_lds_dwordx4 v[12:13], off
	v_add_u32_e32 v15, 0xc000, v6
	s_mov_b64 s[2:3], 0xc000
	v_lshl_add_u64 v[12:13], v[8:9], 0, s[2:3]
	v_readfirstlane_b32 s4, v15
	s_mov_b32 m0, s4
	s_nop 0
	global_load_lds_dwordx4 v[12:13], off
	v_add_u32_e32 v15, 0xf000, v6
	s_mov_b64 s[2:3], 0xf000
	v_lshl_add_u64 v[12:13], v[8:9], 0, s[2:3]
	v_readfirstlane_b32 s4, v15
	s_mov_b32 m0, s4
	s_nop 0
	global_load_lds_dwordx4 v[12:13], off
	s_mov_b32 s2, 0x14400
	v_mul_u32_u24_e32 v4, 0x4080, v119
	s_waitcnt vmcnt(6)
	v_add3_u32 v5, v108, v4, s2
	v_lshl_or_b32 v4, v118, 2, v4
	s_mov_b64 s[2:3], 0x14280
	s_waitcnt lgkmcnt(0)
	s_barrier
	v_add_u32_e32 v4, 0x18400, v4
	v_lshl_add_u64 v[2:3], v[2:3], 0, s[2:3]
	ds_read_b128 v[88:91], v5
	ds_read_b128 v[84:87], v5 offset:1024
	ds_read_b128 v[80:83], v5 offset:2048
	ds_read_b128 v[76:79], v5 offset:3072
	ds_read_b128 v[72:75], v5 offset:4096
	ds_read_b128 v[68:71], v5 offset:5120
	ds_read_b128 v[64:67], v5 offset:6144
	ds_read_b128 v[60:63], v5 offset:7168
	ds_read_b128 v[56:59], v5 offset:8192
	ds_read_b128 v[52:55], v5 offset:9216
	ds_read_b128 v[48:51], v5 offset:10240
	ds_read_b128 v[44:47], v5 offset:11264
	ds_read_b128 v[40:43], v5 offset:12288
	ds_read_b128 v[36:39], v5 offset:13312
	ds_read_b128 v[32:35], v5 offset:14336
	ds_read_b128 v[28:31], v5 offset:15360
	ds_read_b32 v116, v4
	s_waitcnt lgkmcnt(0)
	v_lshl_add_u64 v[4:5], v[2:3], 0, v[6:7]
	v_add_u32_e32 v7, 0x14280, v6
	s_barrier
	v_readfirstlane_b32 s2, v7
	v_add_u32_e32 v7, 0x17280, v6
	s_mov_b32 m0, s2
	v_mov_b32_e32 v15, v109
	v_readfirstlane_b32 s2, v7
	v_add_u32_e32 v7, 0x1a280, v6
	global_load_lds_dwordx4 v[4:5], off
	v_lshl_add_u64 v[4:5], v[2:3], 0, v[14:15]
	s_mov_b32 m0, s2
	v_mov_b32_e32 v17, v109
	v_readfirstlane_b32 s2, v7
	v_add_u32_e32 v7, 0x1d280, v6
	global_load_lds_dwordx4 v[4:5], off
	v_lshl_add_u64 v[4:5], v[2:3], 0, v[16:17]
	s_mov_b32 m0, s2
	v_mov_b32_e32 v19, v109
	v_readfirstlane_b32 s2, v7
	global_load_lds_dwordx4 v[4:5], off
	v_lshl_add_u64 v[4:5], v[2:3], 0, v[18:19]
	s_mov_b32 m0, s2
	v_bfe_u32 v117, v0, 5, 1
	global_load_lds_dwordx4 v[4:5], off
	v_or_b32_e32 v4, 0xc000, v6
	v_add_u32_e32 v6, 0x20280, v6
	v_mov_b32_e32 v5, v109
	v_readfirstlane_b32 s2, v6
	v_lshl_add_u64 v[4:5], v[2:3], 0, v[4:5]
	s_mov_b32 m0, s2
	v_add_u32_e32 v131, 33, v115
	global_load_lds_dwordx4 v[4:5], off
	v_min_u32_e32 v4, 4, v27
	v_lshlrev_b32_e32 v6, 10, v4
	v_add_u32_e32 v4, 0xf000, v6
	v_mov_b32_e32 v5, v109
	v_lshl_add_u64 v[2:3], v[2:3], 0, v[4:5]
	v_add_u32_e32 v4, 0x23280, v6
	s_movk_i32 s73, 0x4080
	v_readfirstlane_b32 s2, v4
	s_mov_b32 m0, s2
	v_mov_b32_e32 v18, 0x7f800000
	global_load_lds_dwordx4 v[2:3], off
	v_mul_u32_u24_e32 v2, 0x4080, v115
	v_lshl_or_b32 v2, v117, 4, v2
	v_add_u32_e32 v132, 0x4000, v2
	v_lshl_or_b32 v2, s59, 2, v119
	v_sub_u32_e32 v134, v2, v115
	v_add_u32_e32 v2, s72, v131
	v_ashrrev_i32_e32 v3, 31, v2
	v_lshlrev_b64 v[2:3], 10, v[2:3]
	v_lshl_or_b32 v2, v1, 2, v2
	v_lshl_add_u64 v[110:111], s[0:1], 0, v[108:109]
	v_cmp_gt_i32_e64 s[0:1], s78, v131
	v_mad_u32_u24 v133, v115, s73, v108
	v_lshl_add_u64 v[112:113], s[60:61], 0, v[2:3]
	s_mov_b64 s[60:61], -1
	v_mov_b32_e32 v135, 0x4080
	v_mov_b32_e32 v136, 0xff800000
	v_mov_b32_e32 v137, 0
	s_mov_b32 s81, s79
	v_mov_b32_e32 v1, v18
	v_mov_b32_e32 v20, v18
	v_mov_b32_e32 v19, v18
	v_mov_b32_e32 v24, v18
	v_mov_b32_e32 v23, v18
	v_mov_b32_e32 v22, v18
	v_mov_b32_e32 v21, v18
	v_mov_b32_e32 v26, v18
	v_mov_b32_e32 v25, v18
	s_waitcnt vmcnt(7)
	s_barrier
	s_branch .LBB1_6

.LBB1_18:
	v_cmp_lt_u32_e32 vcc, v139, v108
	s_and_saveexec_b64 s[72:73], vcc
	s_cbranch_execz .LBB1_11
	v_add_u32_e32 v141, s82, v133
	ds_read_b128 v[2:5], v141
	ds_read_b128 v[92:95], v141 offset:1024
	ds_read_b128 v[96:99], v141 offset:2048
	ds_read_b128 v[100:103], v141 offset:3072
	ds_read_b128 v[104:107], v141 offset:4096
	ds_read_b128 v[142:145], v141 offset:5120
	ds_read_b128 v[146:149], v141 offset:6144
	ds_read_b128 v[150:153], v141 offset:7168
	ds_read_b128 v[154:157], v141 offset:15360
	v_add_u32_e32 v158, s82, v132
	s_waitcnt lgkmcnt(8)
	v_mfma_f32_32x32x16_f16 v[2:17], v[2:5], v[88:91], 0
	s_waitcnt lgkmcnt(7)
	v_mfma_f32_32x32x16_f16 v[2:17], v[92:95], v[84:87], v[2:17]
	ds_read_b128 v[92:95], v141 offset:8192
	s_waitcnt lgkmcnt(7)
	v_mfma_f32_32x32x16_f16 v[2:17], v[96:99], v[80:83], v[2:17]
	ds_read_b128 v[96:99], v141 offset:9216
	s_waitcnt lgkmcnt(7)
	v_mfma_f32_32x32x16_f16 v[2:17], v[100:103], v[76:79], v[2:17]
	ds_read_b128 v[100:103], v141 offset:10240
	s_waitcnt lgkmcnt(7)
	v_mfma_f32_32x32x16_f16 v[2:17], v[104:107], v[72:75], v[2:17]
	ds_read_b128 v[104:107], v141 offset:11264
	s_waitcnt lgkmcnt(7)
	v_mfma_f32_32x32x16_f16 v[2:17], v[142:145], v[68:71], v[2:17]
	ds_read_b128 v[142:145], v141 offset:12288
	s_waitcnt lgkmcnt(7)
	v_mfma_f32_32x32x16_f16 v[2:17], v[146:149], v[64:67], v[2:17]
	ds_read_b128 v[146:149], v141 offset:13312
	s_waitcnt lgkmcnt(7)
	v_mfma_f32_32x32x16_f16 v[2:17], v[150:153], v[60:63], v[2:17]
	ds_read_b128 v[150:153], v141 offset:14336
	s_waitcnt lgkmcnt(6)
	v_mfma_f32_32x32x16_f16 v[2:17], v[92:95], v[56:59], v[2:17]
	ds_read_b128 v[92:95], v158 offset:96
	s_waitcnt lgkmcnt(6)
	v_mfma_f32_32x32x16_f16 v[2:17], v[96:99], v[52:55], v[2:17]
	ds_read_b128 v[96:99], v158 offset:64
	s_waitcnt lgkmcnt(6)
	v_mfma_f32_32x32x16_f16 v[2:17], v[100:103], v[48:51], v[2:17]
	ds_read_b128 v[100:103], v158 offset:32
	s_waitcnt lgkmcnt(6)
	v_mfma_f32_32x32x16_f16 v[2:17], v[104:107], v[44:47], v[2:17]
	ds_read_b128 v[104:107], v158
	s_waitcnt lgkmcnt(6)
	v_mfma_f32_32x32x16_f16 v[2:17], v[142:145], v[40:43], v[2:17]
	s_waitcnt lgkmcnt(5)
	v_mfma_f32_32x32x16_f16 v[2:17], v[146:149], v[36:39], v[2:17]
	s_waitcnt lgkmcnt(4)
	v_mfma_f32_32x32x16_f16 v[2:17], v[150:153], v[32:35], v[2:17]
	v_mfma_f32_32x32x16_f16 v[2:17], v[154:157], v[28:31], v[2:17]
	s_waitcnt lgkmcnt(0)
	s_nop 3
	v_cmp_eq_u32_e32 vcc, s81, v140
	s_and_saveexec_b64 s[74:75], vcc
	s_cbranch_execz .LBB1_10
	s_nop 7
	v_lshrrev_b32_e32 v142, 1, v0
	v_and_b32_e32 v143, 3, v0
	v_and_or_b32 v142, v142, 12, v143
	v_bfe_u32 v143, v0, 2, 1
	v_cmp_eq_u32_e32 vcc, v117, v143
	v_mov_b32_e32 v143, 0xff
	s_nop 1
	v_cndmask_b32_e32 v142, v143, v142, vcc
	v_cmp_eq_u32_e64 s[84:85], 0, v142
	v_cmp_eq_u32_e64 s[86:87], 1, v142
	v_cmp_eq_u32_e64 s[88:89], 2, v142
	v_cndmask_b32_e64 v2, v2, v136, s[84:85]
	v_cmp_eq_u32_e64 s[84:85], 3, v142
	v_cndmask_b32_e64 v3, v3, v136, s[86:87]
	v_cmp_eq_u32_e64 s[86:87], 4, v142
	v_cndmask_b32_e64 v4, v4, v136, s[88:89]
	v_cmp_eq_u32_e64 s[88:89], 5, v142
	v_cndmask_b32_e64 v5, v5, v136, s[84:85]
	v_cmp_eq_u32_e64 s[84:85], 6, v142
	v_cndmask_b32_e64 v6, v6, v136, s[86:87]
	v_cmp_eq_u32_e64 s[86:87], 7, v142
	v_cndmask_b32_e64 v7, v7, v136, s[88:89]
	v_cmp_eq_u32_e64 s[88:89], 8, v142
	v_cndmask_b32_e64 v8, v8, v136, s[84:85]
	v_cmp_eq_u32_e64 s[84:85], 9, v142
	v_cndmask_b32_e64 v9, v9, v136, s[86:87]
	v_cmp_eq_u32_e64 s[86:87], 10, v142
	v_cndmask_b32_e64 v10, v10, v136, s[88:89]
	v_cmp_eq_u32_e64 s[88:89], 11, v142
	v_cndmask_b32_e64 v11, v11, v136, s[84:85]
	v_cmp_eq_u32_e64 s[84:85], 12, v142
	v_cndmask_b32_e64 v12, v12, v136, s[86:87]
	v_cmp_eq_u32_e64 s[86:87], 13, v142
	v_cndmask_b32_e64 v13, v13, v136, s[88:89]
	v_cmp_eq_u32_e64 s[88:89], 14, v142
	v_cndmask_b32_e64 v14, v14, v136, s[84:85]
	v_cmp_eq_u32_e64 s[84:85], 15, v142
	v_cndmask_b32_e64 v15, v15, v136, s[86:87]
	v_cndmask_b32_e64 v16, v16, v136, s[88:89]
	v_cndmask_b32_e64 v17, v17, v136, s[84:85]
	s_branch .LBB1_10
.LBB1_21:
	s_waitcnt vmcnt(0)
	s_and_b64 s[60:61], s[68:69], s[60:61]
	s_andn2_b64 vcc, exec, s[60:61]
	s_cbranch_vccnz .LBB1_5
	s_waitcnt vmcnt(0)
	v_sub_u32_e32 v142, s78, v115
	v_cmp_lt_i32_e64 s[36:37], 0, v142
	v_cmp_lt_i32_e64 s[38:39], 3, v142
	v_cmp_lt_i32_e64 s[40:41], 6, v142
	v_cmp_lt_i32_e64 s[42:43], 9, v142
	v_cmp_lt_i32_e64 s[44:45], 12, v142
	v_cmp_lt_i32_e64 s[46:47], 15, v142
	v_cmp_lt_i32_e64 s[48:49], 18, v142
	v_cmp_lt_i32_e64 s[50:51], 21, v142
	v_cmp_lt_i32_e64 s[52:53], 24, v142
	v_cmp_lt_i32_e64 s[54:55], 27, v142
	v_cmp_lt_i32_e64 s[56:57], 30, v142
	v_mov_b32_e32 v2, v120
	v_mov_b32_e32 v3, v121
	v_add_f32_e32 v2, 0, v2
	v_cndmask_b32_e64 v2, 0, v2, s[36:37]
	v_cndmask_b32_e64 v3, 0, v3, s[38:39]
	v_add_f32_e32 v2, v2, v3
	v_mov_b32_e32 v3, v122
	s_nop 0
	v_cndmask_b32_e64 v3, 0, v3, s[40:41]
	v_add_f32_e32 v2, v2, v3
	v_mov_b32_e32 v3, v123
	s_nop 0
	v_cndmask_b32_e64 v3, 0, v3, s[42:43]
	v_add_f32_e32 v2, v2, v3
	v_mov_b32_e32 v3, v124
	s_nop 0
	v_cndmask_b32_e64 v3, 0, v3, s[44:45]
	v_add_f32_e32 v2, v2, v3
	v_mov_b32_e32 v3, v125
	s_nop 0
	v_cndmask_b32_e64 v3, 0, v3, s[46:47]
	v_add_f32_e32 v2, v2, v3
	v_mov_b32_e32 v3, v126
	s_nop 0
	v_cndmask_b32_e64 v3, 0, v3, s[48:49]
	v_add_f32_e32 v2, v2, v3
	v_mov_b32_e32 v3, v127
	s_nop 0
	v_cndmask_b32_e64 v3, 0, v3, s[50:51]
	v_add_f32_e32 v2, v2, v3
	v_mov_b32_e32 v3, v128
	s_nop 0
	v_cndmask_b32_e64 v3, 0, v3, s[52:53]
	v_add_f32_e32 v2, v2, v3
	v_mov_b32_e32 v3, v129
	s_nop 0
	v_cndmask_b32_e64 v3, 0, v3, s[54:55]
	v_add_f32_e32 v2, v2, v3
	v_mov_b32_e32 v3, v130
	s_nop 0
	v_cndmask_b32_e64 v3, 0, v3, s[56:57]
	v_add_f32_e32 v137, v2, v3
	s_and_saveexec_b64 s[60:61], s[0:1]
	s_cbranch_execz .LBB1_4
	s_mov_b64 s[72:73], 0
	v_mov_b64_e32 v[2:3], v[112:113]
	v_mov_b32_e32 v4, v131
